# HGRN2 chain: static priority 1 for the two waves that run the intra-chunk output chain (waves 0-1), reset at chain end
# baseline (speedup 1.0000x reference)
.LBB0_293:
	s_setprio 0
	v_readlane_b32 s86, v255, 33
	s_add_i32 s2, s2, s86
	v_readlane_b32 s87, v255, 34
	s_cmp_gt_i32 s2, 31
	s_barrier
	s_barrier
	s_cbranch_scc1 .LBB0_279
.LBB0_294:
	v_readfirstlane_b32 s0, v0
	s_nop 3
	s_cmp_lt_u32 s0, 0x80
	s_cbranch_scc0 .Lhgp_skip
	s_setprio 1
